# MoE expert GEMMs (gate|up, down): MFMA blocks of 64-row wave slices that hold only padding rows are skipped (slice's first row->token entry read per unit)
# baseline (speedup 1.0000x reference)
; #define PG8_STAGE(bufoff, gbase, voff) do { _Pragma("unroll") for (int _i = 0; _i < 2; ++_i) \
;         __builtin_amdgcn_global_load_lds((const unsigned*)((const char*)(gbase) + (voff)[_i]), (LAS unsigned*)(lds + (bufoff) + ldsw + _i * 8192), 16, 0, 0); } while (0)
; #define PG8_LDA(dst, b, h) do { _Pragma("unroll") for (int m = 0; m < 4; ++m) _Pragma("unroll") for (int k = 0; k < 2; ++k) dst[m][k] = *(const LAS bf16x8*)(lds + PG8_SA(b, h) + aoff + m * 2048 + k * KOFF); } while (0)
; #define PG8_LDB(dst, b, h) do { _Pragma("unroll") for (int n = 0; n < 2; ++n) _Pragma("unroll") for (int k = 0; k < 2; ++k) dst[n][k] = *(const LAS bf16x8*)(lds + PG8_SB(b, h) + boff + n * 2048 + k * KOFF); } while (0)
; #define PG8_WAIT_V(n) asm volatile("s_waitcnt vmcnt(" #n ")" ::: "memory")
; #define PG8_WAIT_L(n) asm volatile("s_waitcnt lgkmcnt(" #n ")" ::: "memory")
; #define PG8_BAR __builtin_amdgcn_s_barrier()
; #define PG8_SCHED __builtin_amdgcn_sched_barrier(0)
; #define PG8_AOFF(u_, o0, o1) do { _Pragma("unroll") for (int _i = 0; _i < 2; ++_i) { const int r0 = (u_).pm * BM + Rr[_i], r1 = r0 + HALF; \
;         const int g0 = GATHER ? g.rowidx[r0] : r0, g1 = GATHER ? g.rowidx[r1] : r1; \
;         o0[_i] = (unsigned)g0 * (unsigned)K + (unsigned)Cc[_i]; o1[_i] = (unsigned)g1 * (unsigned)K + (unsigned)Cc[_i]; } } while (0)
; template <class Epi, class Sched, bool GATHER, bool FP8 = false, bool ALIGN = true>
; __device__ __forceinline__ void gemm_phase(LAS unsigned char* lds, int wave, const Gemm g, const Sched& S, const Epi& E) {
;     ...
;             PG8_LDB(B0, 0, 0); PG8_LDB(B1, 0, 1); PG8_SCHED; PG8_LDA(At, 0, 0); PG8_STAGE(PG8_SA(1, 1), a1, ca1);
;             if (last && has_next) PG8_AOFF(nxt, ca0, ca1);
;             PG8_WAIT_V(8); PG8_WAIT_L(0); PG8_BAR; PG8_MMA(0, 0, At, B0); PG8_MMA(0, 1, At, B1); PG8_BAR; PG8_SCHED;
;             PG8_LDA(At, 0, 1); PG8_STAGE(PG8_SB(0, 0), b2, voffB0); PG8_STAGE(PG8_SB(0, 1), b2, voffB1); PG8_STAGE(PG8_SA(0, 0), a2, ca0);
.Lpeel_gu_h:
	v_readlane_b32 s100, v255, 7
	s_lshr_b32 s100, s100, 2
	s_lshl_b32 s100, s100, 8
	s_lshl_b32 s101, s79, 10
	s_add_u32 s100, s100, s101
	s_add_u32 s100, s100, 0x200
	s_add_u32 s100, s36, s100
	s_addc_u32 s101, s37, 0
	v_mov_b32_e32 v244, s100
	v_mov_b32_e32 v245, s101
	global_load_dword v246, v[244:245], off
	v_add_u32_e32 v0, 0, v236
	v_add_u32_e32 v1, 0x10000, v0
	v_add_u32_e32 v12, 0x14000, v0
	ds_read_b128 v[16:19], v1
	ds_read_b128 v[20:23], v1 offset:1024
	ds_read_b128 v[24:27], v1 offset:2048
	ds_read_b128 v[28:31], v1 offset:3072
	ds_read_b128 v[0:3], v12
	ds_read_b128 v[4:7], v12 offset:1024
	ds_read_b128 v[8:11], v12 offset:2048
	ds_read_b128 v[12:15], v12 offset:3072
	s_cmp_eq_u32 s83, 12
	s_cselect_b64 s[12:13], -1, 0
	s_add_i32 m0, s31, 0xc000
	ds_read_b128 v[56:59], v238
	ds_read_b128 v[60:63], v238 offset:1024
	ds_read_b128 v[48:51], v238 offset:2048
	ds_read_b128 v[52:55], v238 offset:3072
	ds_read_b128 v[40:43], v238 offset:4096
	ds_read_b128 v[44:47], v238 offset:5120
	ds_read_b128 v[32:35], v238 offset:6144
	ds_read_b128 v[36:39], v238 offset:7168
	global_load_lds_dwordx4 v212, s[10:11]
	s_add_i32 m0, s31, 0xe000
	s_and_b64 s[14:15], s[50:51], s[12:13]
	global_load_lds_dwordx4 v216, s[10:11]
	s_andn2_b64 vcc, exec, s[14:15]
	s_cbranch_vccz .Lpeel_gu_a
	v_mov_b32_e32 v213, v193
	s_branch .Lpeel_gu_b

; #define PG8_STAGE(bufoff, gbase, voff) do { _Pragma("unroll") for (int _i = 0; _i < 2; ++_i) \
;         __builtin_amdgcn_global_load_lds((const unsigned*)((const char*)(gbase) + (voff)[_i]), (LAS unsigned*)(lds + (bufoff) + ldsw + _i * 8192), 16, 0, 0); } while (0)
; #define PG8_LDA(dst, b, h) do { _Pragma("unroll") for (int m = 0; m < 4; ++m) _Pragma("unroll") for (int k = 0; k < 2; ++k) dst[m][k] = *(const LAS bf16x8*)(lds + PG8_SA(b, h) + aoff + m * 2048 + k * KOFF); } while (0)
; #define PG8_WAIT_V(n) asm volatile("s_waitcnt vmcnt(" #n ")" ::: "memory")
; #define PG8_WAIT_L(n) asm volatile("s_waitcnt lgkmcnt(" #n ")" ::: "memory")
; #define PG8_BAR __builtin_amdgcn_s_barrier()
; #define PG8_SCHED __builtin_amdgcn_sched_barrier(0)
; template <class Epi, class Sched, bool GATHER, bool FP8 = false, bool ALIGN = true>
; __device__ __forceinline__ void gemm_phase(LAS unsigned char* lds, int wave, const Gemm g, const Sched& S, const Epi& E) {
;     ...
;             PG8_WAIT_V(8); PG8_WAIT_L(0); PG8_BAR; PG8_MMA(0, 0, At, B0); PG8_MMA(0, 1, At, B1); PG8_BAR; PG8_SCHED;
;             PG8_LDA(At, 0, 1); PG8_STAGE(PG8_SB(0, 0), b2, voffB0); PG8_STAGE(PG8_SB(0, 1), b2, voffB1); PG8_STAGE(PG8_SA(0, 0), a2, ca0);
;             PG8_WAIT_V(8); PG8_WAIT_L(0); PG8_BAR; PG8_MMA(1, 0, At, B0); PG8_MMA(1, 1, At, B1); PG8_BAR; PG8_SCHED;
.Lgu_norow:
	s_setprio 1
	s_waitcnt lgkmcnt(0)
	v_mfma_scale_f32_16x16x128_f8f6f4 v[188:191], v[16:23], v[56:63], 0, v252, v251 op_sel_hi:[0,0,0]
	v_mfma_scale_f32_16x16x128_f8f6f4 v[180:183], v[24:31], v[56:63], 0, v252, v251 op_sel_hi:[0,0,0]
	v_mfma_scale_f32_16x16x128_f8f6f4 v[172:175], v[16:23], v[48:55], 0, v252, v251 op_sel_hi:[0,0,0]
	v_mfma_scale_f32_16x16x128_f8f6f4 v[164:167], v[24:31], v[48:55], 0, v252, v251 op_sel_hi:[0,0,0]
	v_mfma_scale_f32_16x16x128_f8f6f4 v[156:159], v[16:23], v[40:47], 0, v252, v251 op_sel_hi:[0,0,0]
	v_mfma_scale_f32_16x16x128_f8f6f4 v[148:151], v[24:31], v[40:47], 0, v252, v251 op_sel_hi:[0,0,0]
	v_mfma_scale_f32_16x16x128_f8f6f4 v[140:143], v[16:23], v[32:39], 0, v252, v251 op_sel_hi:[0,0,0]
	v_mfma_scale_f32_16x16x128_f8f6f4 v[132:135], v[24:31], v[32:39], 0, v252, v251 op_sel_hi:[0,0,0]
	s_setprio 0
	s_setprio 1
	v_mfma_scale_f32_16x16x128_f8f6f4 v[184:187], v[0:7], v[56:63], 0, v252, v251 op_sel_hi:[0,0,0]
	v_mfma_scale_f32_16x16x128_f8f6f4 v[176:179], v[8:15], v[56:63], 0, v252, v251 op_sel_hi:[0,0,0]
	v_mfma_scale_f32_16x16x128_f8f6f4 v[168:171], v[0:7], v[48:55], 0, v252, v251 op_sel_hi:[0,0,0]
	v_mfma_scale_f32_16x16x128_f8f6f4 v[160:163], v[8:15], v[48:55], 0, v252, v251 op_sel_hi:[0,0,0]
	v_mfma_scale_f32_16x16x128_f8f6f4 v[152:155], v[0:7], v[40:47], 0, v252, v251 op_sel_hi:[0,0,0]
	v_mfma_scale_f32_16x16x128_f8f6f4 v[144:147], v[8:15], v[40:47], 0, v252, v251 op_sel_hi:[0,0,0]
	v_mfma_scale_f32_16x16x128_f8f6f4 v[136:139], v[0:7], v[32:39], 0, v252, v251 op_sel_hi:[0,0,0]
	v_mfma_scale_f32_16x16x128_f8f6f4 v[128:131], v[8:15], v[32:39], 0, v252, v251 op_sel_hi:[0,0,0]
	s_setprio 0
	s_barrier
	s_mov_b32 m0, s34
	v_lshl_add_u64 v[196:197], s[14:15], 0, v[204:205]
	ds_read_b128 v[32:35], v238 offset:16384
	ds_read_b128 v[36:39], v238 offset:17408
	ds_read_b128 v[40:43], v238 offset:18432
	ds_read_b128 v[44:47], v238 offset:19456
	ds_read_b128 v[48:51], v238 offset:20480
	ds_read_b128 v[52:55], v238 offset:21504
	ds_read_b128 v[56:59], v238 offset:22528
	ds_read_b128 v[60:63], v238 offset:23552
	global_load_lds_dwordx4 v[196:197], off
	v_lshl_add_u64 v[198:199], s[14:15], 0, v[208:209]
	s_mov_b32 m0, s35
	v_lshl_add_u64 v[200:201], s[14:15], 0, v[206:207]
	global_load_lds_dwordx4 v[198:199], off
	s_mov_b32 m0, s40
	v_lshl_add_u64 v[202:203], s[14:15], 0, v[210:211]
	global_load_lds_dwordx4 v[200:201], off
	s_mov_b32 m0, s41
	v_mov_b32_e32 v215, v193
	global_load_lds_dwordx4 v[202:203], off
	s_mov_b32 m0, s31
	v_lshl_add_u64 v[226:227], s[12:13], 0, v[192:193]
	global_load_lds_dwordx4 v192, s[12:13]
	s_mov_b32 m0, s53
	v_lshl_add_u64 v[228:229], s[12:13], 0, v[214:215]
	global_load_lds_dwordx4 v214, s[12:13]
	s_waitcnt vmcnt(8)
	s_waitcnt lgkmcnt(0)
	s_barrier
	s_setprio 1
	s_waitcnt lgkmcnt(0)
	v_readfirstlane_b32 s101, v246
	s_cmp_eq_u32 s101, 0
	s_cbranch_scc1 .Lpad_gu_0
	v_mfma_scale_f32_16x16x128_f8f6f4 v[124:127], v[16:23], v[32:39], 0, v252, v251 op_sel_hi:[0,0,0]
	v_mfma_scale_f32_16x16x128_f8f6f4 v[116:119], v[24:31], v[32:39], 0, v252, v251 op_sel_hi:[0,0,0]
	v_mfma_scale_f32_16x16x128_f8f6f4 v[108:111], v[16:23], v[40:47], 0, v252, v251 op_sel_hi:[0,0,0]
	v_mfma_scale_f32_16x16x128_f8f6f4 v[100:103], v[24:31], v[40:47], 0, v252, v251 op_sel_hi:[0,0,0]
	v_mfma_scale_f32_16x16x128_f8f6f4 v[92:95], v[16:23], v[48:55], 0, v252, v251 op_sel_hi:[0,0,0]
	v_mfma_scale_f32_16x16x128_f8f6f4 v[84:87], v[24:31], v[48:55], 0, v252, v251 op_sel_hi:[0,0,0]
	v_mfma_scale_f32_16x16x128_f8f6f4 v[76:79], v[16:23], v[56:63], 0, v252, v251 op_sel_hi:[0,0,0]
	v_mfma_scale_f32_16x16x128_f8f6f4 v[68:71], v[24:31], v[56:63], 0, v252, v251 op_sel_hi:[0,0,0]
.Lpad_gu_0:
	s_setprio 0
	s_setprio 1
	s_cmp_eq_u32 s101, 0
	s_cbranch_scc1 .Lpad_gu_1
	v_mfma_scale_f32_16x16x128_f8f6f4 v[120:123], v[0:7], v[32:39], 0, v252, v251 op_sel_hi:[0,0,0]
	v_mfma_scale_f32_16x16x128_f8f6f4 v[112:115], v[8:15], v[32:39], 0, v252, v251 op_sel_hi:[0,0,0]
	v_mfma_scale_f32_16x16x128_f8f6f4 v[104:107], v[0:7], v[40:47], 0, v252, v251 op_sel_hi:[0,0,0]
	v_mfma_scale_f32_16x16x128_f8f6f4 v[96:99], v[8:15], v[40:47], 0, v252, v251 op_sel_hi:[0,0,0]
	v_mfma_scale_f32_16x16x128_f8f6f4 v[88:91], v[0:7], v[48:55], 0, v252, v251 op_sel_hi:[0,0,0]
	v_mfma_scale_f32_16x16x128_f8f6f4 v[80:83], v[8:15], v[48:55], 0, v252, v251 op_sel_hi:[0,0,0]
	v_mfma_scale_f32_16x16x128_f8f6f4 v[72:75], v[0:7], v[56:63], 0, v252, v251 op_sel_hi:[0,0,0]
	v_mfma_scale_f32_16x16x128_f8f6f4 v[64:67], v[8:15], v[56:63], 0, v252, v251 op_sel_hi:[0,0,0]
; #define PG8_STAGE(bufoff, gbase, voff) do { _Pragma("unroll") for (int _i = 0; _i < 2; ++_i) \
;         __builtin_amdgcn_global_load_lds((const unsigned*)((const char*)(gbase) + (voff)[_i]), (LAS unsigned*)(lds + (bufoff) + ldsw + _i * 8192), 16, 0, 0); } while (0)
; #define PG8_LDA(dst, b, h) do { _Pragma("unroll") for (int m = 0; m < 4; ++m) _Pragma("unroll") for (int k = 0; k < 2; ++k) dst[m][k] = *(const LAS bf16x8*)(lds + PG8_SA(b, h) + aoff + m * 2048 + k * KOFF); } while (0)
; #define PG8_LDB(dst, b, h) do { _Pragma("unroll") for (int n = 0; n < 2; ++n) _Pragma("unroll") for (int k = 0; k < 2; ++k) dst[n][k] = *(const LAS bf16x8*)(lds + PG8_SB(b, h) + boff + n * 2048 + k * KOFF); } while (0)
; #define PG8_WAIT_V(n) asm volatile("s_waitcnt vmcnt(" #n ")" ::: "memory")
; #define PG8_WAIT_L(n) asm volatile("s_waitcnt lgkmcnt(" #n ")" ::: "memory")
; #define PG8_BAR __builtin_amdgcn_s_barrier()
; #define PG8_SCHED __builtin_amdgcn_sched_barrier(0)
; template <class Epi, class Sched, bool GATHER, bool FP8 = false, bool ALIGN = true>
; __device__ __forceinline__ void gemm_phase(LAS unsigned char* lds, int wave, const Gemm g, const Sched& S, const Epi& E) {
;     ...
;             PG8_LDB(B0, 1, 0); PG8_LDB(B1, 1, 1); PG8_SCHED; PG8_LDA(At, 1, 0); PG8_STAGE(PG8_SA(0, 1), a2, ca1);
;             PG8_WAIT_V(8); PG8_WAIT_L(0); PG8_BAR; PG8_MMA(0, 0, At, B0); PG8_MMA(0, 1, At, B1); PG8_BAR; PG8_SCHED;
;             PG8_LDA(At, 1, 1); PG8_STAGE(PG8_SB(1, 0), b3, voffB0); PG8_STAGE(PG8_SB(1, 1), b3, voffB1); PG8_STAGE(PG8_SA(1, 0), a3, ca0);
;             PG8_WAIT_V(8); PG8_WAIT_L(0); PG8_BAR; PG8_MMA(1, 0, At, B0); PG8_MMA(1, 1, At, B1); PG8_BAR; PG8_SCHED;
.Lpad_gu_1:
	s_setprio 0
	s_barrier
	s_add_i32 s14, 0, 0x18000
	s_add_i32 s15, 0, 0x1c000
	v_add_u32_e32 v12, s14, v236
	v_add_u32_e32 v28, s15, v236
	ds_read_b128 v[0:3], v12
	ds_read_b128 v[4:7], v12 offset:1024
	ds_read_b128 v[8:11], v12 offset:2048
	ds_read_b128 v[12:15], v12 offset:3072
	ds_read_b128 v[16:19], v28
	ds_read_b128 v[20:23], v28 offset:1024
	ds_read_b128 v[24:27], v28 offset:2048
	ds_read_b128 v[28:31], v28 offset:3072
	s_mov_b32 m0, s56
	v_lshl_add_u64 v[230:231], s[12:13], 0, v[212:213]
	ds_read_b128 v[32:35], v238 offset:32768
	ds_read_b128 v[36:39], v238 offset:33792
	ds_read_b128 v[40:43], v238 offset:34816
	ds_read_b128 v[44:47], v238 offset:35840
	ds_read_b128 v[48:51], v238 offset:36864
	ds_read_b128 v[52:55], v238 offset:37888
	ds_read_b128 v[56:59], v238 offset:38912
	ds_read_b128 v[60:63], v238 offset:39936
	global_load_lds_dwordx4 v[230:231], off
	v_lshl_add_u64 v[230:231], s[12:13], 0, v[216:217]
	s_mov_b32 m0, s57
	s_nop 0
	global_load_lds_dwordx4 v[230:231], off
	s_waitcnt vmcnt(8)
	s_waitcnt lgkmcnt(0)
	s_barrier
	s_setprio 1
	s_waitcnt lgkmcnt(0)
	v_mfma_scale_f32_16x16x128_f8f6f4 v[188:191], v[0:7], v[32:39], v[188:191], v252, v251 op_sel_hi:[0,0,0]
	v_mfma_scale_f32_16x16x128_f8f6f4 v[180:183], v[8:15], v[32:39], v[180:183], v252, v251 op_sel_hi:[0,0,0]
	v_mfma_scale_f32_16x16x128_f8f6f4 v[172:175], v[0:7], v[40:47], v[172:175], v252, v251 op_sel_hi:[0,0,0]
	v_mfma_scale_f32_16x16x128_f8f6f4 v[164:167], v[8:15], v[40:47], v[164:167], v252, v251 op_sel_hi:[0,0,0]
	v_mfma_scale_f32_16x16x128_f8f6f4 v[156:159], v[0:7], v[48:55], v[156:159], v252, v251 op_sel_hi:[0,0,0]
	v_mfma_scale_f32_16x16x128_f8f6f4 v[148:151], v[8:15], v[48:55], v[148:151], v252, v251 op_sel_hi:[0,0,0]
	v_mfma_scale_f32_16x16x128_f8f6f4 v[140:143], v[0:7], v[56:63], v[140:143], v252, v251 op_sel_hi:[0,0,0]
	v_mfma_scale_f32_16x16x128_f8f6f4 v[132:135], v[8:15], v[56:63], v[132:135], v252, v251 op_sel_hi:[0,0,0]
	s_setprio 0
	s_setprio 1
	v_mfma_scale_f32_16x16x128_f8f6f4 v[184:187], v[16:23], v[32:39], v[184:187], v252, v251 op_sel_hi:[0,0,0]
	v_mfma_scale_f32_16x16x128_f8f6f4 v[176:179], v[24:31], v[32:39], v[176:179], v252, v251 op_sel_hi:[0,0,0]
	v_mfma_scale_f32_16x16x128_f8f6f4 v[168:171], v[16:23], v[40:47], v[168:171], v252, v251 op_sel_hi:[0,0,0]
	v_mfma_scale_f32_16x16x128_f8f6f4 v[160:163], v[24:31], v[40:47], v[160:163], v252, v251 op_sel_hi:[0,0,0]
	v_mfma_scale_f32_16x16x128_f8f6f4 v[152:155], v[16:23], v[48:55], v[152:155], v252, v251 op_sel_hi:[0,0,0]
	v_mfma_scale_f32_16x16x128_f8f6f4 v[144:147], v[24:31], v[48:55], v[144:147], v252, v251 op_sel_hi:[0,0,0]
	v_mfma_scale_f32_16x16x128_f8f6f4 v[136:139], v[16:23], v[56:63], v[136:139], v252, v251 op_sel_hi:[0,0,0]
	v_mfma_scale_f32_16x16x128_f8f6f4 v[128:131], v[24:31], v[56:63], v[128:131], v252, v251 op_sel_hi:[0,0,0]
	s_setprio 0
	s_barrier
	s_add_i32 s12, s14, s30
	v_lshl_add_u64 v[196:197], v[196:197], 0, s[62:63]
	s_mov_b32 m0, s12
	ds_read_b128 v[32:35], v238 offset:49152
	ds_read_b128 v[36:39], v238 offset:50176
	ds_read_b128 v[40:43], v238 offset:51200
	ds_read_b128 v[44:47], v238 offset:52224
	ds_read_b128 v[48:51], v238 offset:53248
	ds_read_b128 v[52:55], v238 offset:54272
	ds_read_b128 v[56:59], v238 offset:55296
	ds_read_b128 v[60:63], v238 offset:56320
	global_load_lds_dwordx4 v[196:197], off
	v_lshl_add_u64 v[196:197], v[198:199], 0, s[62:63]
	s_add_i32 m0, s12, 0x2000
	s_add_i32 s12, s15, s30
	global_load_lds_dwordx4 v[196:197], off
	v_lshl_add_u64 v[196:197], v[200:201], 0, s[62:63]
	s_mov_b32 m0, s12
	s_nop 0
	global_load_lds_dwordx4 v[196:197], off
	v_lshl_add_u64 v[196:197], v[202:203], 0, s[62:63]
	s_add_i32 m0, s12, 0x2000
	s_nop 0
	global_load_lds_dwordx4 v[196:197], off
	v_lshl_add_u64 v[196:197], v[226:227], 0, s[62:63]
	s_mov_b32 m0, s58
	s_nop 0
	global_load_lds_dwordx4 v[196:197], off
	v_lshl_add_u64 v[196:197], v[228:229], 0, s[62:63]
	s_mov_b32 m0, s59
	s_nop 0
	global_load_lds_dwordx4 v[196:197], off
	s_waitcnt vmcnt(8)
	s_waitcnt lgkmcnt(0)
	s_barrier
	s_setprio 1
	s_waitcnt lgkmcnt(0)
	s_cmp_eq_u32 s101, 0
	s_cbranch_scc1 .Lpad_gu_2
	v_mfma_scale_f32_16x16x128_f8f6f4 v[124:127], v[0:7], v[32:39], v[124:127], v252, v251 op_sel_hi:[0,0,0]
	v_mfma_scale_f32_16x16x128_f8f6f4 v[116:119], v[8:15], v[32:39], v[116:119], v252, v251 op_sel_hi:[0,0,0]
	v_mfma_scale_f32_16x16x128_f8f6f4 v[108:111], v[0:7], v[40:47], v[108:111], v252, v251 op_sel_hi:[0,0,0]
	v_mfma_scale_f32_16x16x128_f8f6f4 v[100:103], v[8:15], v[40:47], v[100:103], v252, v251 op_sel_hi:[0,0,0]
	v_mfma_scale_f32_16x16x128_f8f6f4 v[92:95], v[0:7], v[48:55], v[92:95], v252, v251 op_sel_hi:[0,0,0]
	v_mfma_scale_f32_16x16x128_f8f6f4 v[84:87], v[8:15], v[48:55], v[84:87], v252, v251 op_sel_hi:[0,0,0]
	v_mfma_scale_f32_16x16x128_f8f6f4 v[76:79], v[0:7], v[56:63], v[76:79], v252, v251 op_sel_hi:[0,0,0]
	v_mfma_scale_f32_16x16x128_f8f6f4 v[68:71], v[8:15], v[56:63], v[68:71], v252, v251 op_sel_hi:[0,0,0]
.Lpad_gu_2:
	s_setprio 0
	s_setprio 1
	s_cmp_eq_u32 s101, 0
	s_cbranch_scc1 .Lpad_gu_3
	v_mfma_scale_f32_16x16x128_f8f6f4 v[120:123], v[16:23], v[32:39], v[120:123], v252, v251 op_sel_hi:[0,0,0]
	v_mfma_scale_f32_16x16x128_f8f6f4 v[112:115], v[24:31], v[32:39], v[112:115], v252, v251 op_sel_hi:[0,0,0]
	v_mfma_scale_f32_16x16x128_f8f6f4 v[104:107], v[16:23], v[40:47], v[104:107], v252, v251 op_sel_hi:[0,0,0]
	v_mfma_scale_f32_16x16x128_f8f6f4 v[96:99], v[24:31], v[40:47], v[96:99], v252, v251 op_sel_hi:[0,0,0]
	v_mfma_scale_f32_16x16x128_f8f6f4 v[88:91], v[16:23], v[48:55], v[88:91], v252, v251 op_sel_hi:[0,0,0]
	v_mfma_scale_f32_16x16x128_f8f6f4 v[80:83], v[24:31], v[48:55], v[80:83], v252, v251 op_sel_hi:[0,0,0]
	v_mfma_scale_f32_16x16x128_f8f6f4 v[72:75], v[16:23], v[56:63], v[72:75], v252, v251 op_sel_hi:[0,0,0]
	v_mfma_scale_f32_16x16x128_f8f6f4 v[64:67], v[24:31], v[56:63], v[64:67], v252, v251 op_sel_hi:[0,0,0]
.Lpad_gu_3:
	s_setprio 0
	s_barrier
	s_add_i32 s83, s83, 2
	s_add_u32 s10, s10, 0x100
	s_addc_u32 s11, s11, 0
	s_add_u32 s49, s49, 0x100
	s_addc_u32 s82, s82, 0
	s_cmp_gt_u32 s83, 13
	s_cbranch_scc1 .LBB0_1083
	s_branch .LBB0_1081

; #define PG8_STAGE(bufoff, gbase, voff) do { _Pragma("unroll") for (int _i = 0; _i < 2; ++_i) \
;         __builtin_amdgcn_global_load_lds((const unsigned*)((const char*)(gbase) + (voff)[_i]), (LAS unsigned*)(lds + (bufoff) + ldsw + _i * 8192), 16, 0, 0); } while (0)
; #define PG8_LDA(dst, b, h) do { _Pragma("unroll") for (int m = 0; m < 4; ++m) _Pragma("unroll") for (int k = 0; k < 2; ++k) dst[m][k] = *(const LAS bf16x8*)(lds + PG8_SA(b, h) + aoff + m * 2048 + k * KOFF); } while (0)
; #define PG8_WAIT_V(n) asm volatile("s_waitcnt vmcnt(" #n ")" ::: "memory")
; #define PG8_WAIT_L(n) asm volatile("s_waitcnt lgkmcnt(" #n ")" ::: "memory")
; #define PG8_BAR __builtin_amdgcn_s_barrier()
; #define PG8_SCHED __builtin_amdgcn_sched_barrier(0)
; template <class Epi, class Sched, bool GATHER, bool FP8 = false, bool ALIGN = true>
; __device__ __forceinline__ void gemm_phase(LAS unsigned char* lds, int wave, const Gemm g, const Sched& S, const Epi& E) {
;     ...
;             PG8_WAIT_V(8); PG8_WAIT_L(0); PG8_BAR; PG8_MMA(0, 0, At, B0); PG8_MMA(0, 1, At, B1); PG8_BAR; PG8_SCHED;
;             PG8_LDA(At, 0, 1); PG8_STAGE(PG8_SB(0, 0), b2, voffB0); PG8_STAGE(PG8_SB(0, 1), b2, voffB1); PG8_STAGE(PG8_SA(0, 0), a2, ca0);
;             PG8_WAIT_V(8); PG8_WAIT_L(0); PG8_BAR; PG8_MMA(1, 0, At, B0); PG8_MMA(1, 1, At, B1); PG8_BAR; PG8_SCHED;
.LBB0_1080:
	s_waitcnt vmcnt(8)
	s_add_u32 s14, s10, 0x80
	s_waitcnt lgkmcnt(0)
	s_addc_u32 s15, s11, 0
	s_and_b64 s[12:13], s[12:13], exec
	v_mov_b32_e32 v217, v193
	s_cselect_b32 s13, s7, s15
	s_cselect_b32 s12, s6, s14
	s_cselect_b32 s15, s5, s82
	s_cselect_b32 s14, s9, s49
	s_barrier
	s_setprio 1
	s_waitcnt lgkmcnt(0)
	v_mfma_scale_f32_16x16x128_f8f6f4 v[188:191], v[16:23], v[56:63], v[188:191], v252, v251 op_sel_hi:[0,0,0]
	v_mfma_scale_f32_16x16x128_f8f6f4 v[180:183], v[24:31], v[56:63], v[180:183], v252, v251 op_sel_hi:[0,0,0]
	v_mfma_scale_f32_16x16x128_f8f6f4 v[172:175], v[16:23], v[48:55], v[172:175], v252, v251 op_sel_hi:[0,0,0]
	v_mfma_scale_f32_16x16x128_f8f6f4 v[164:167], v[24:31], v[48:55], v[164:167], v252, v251 op_sel_hi:[0,0,0]
	v_mfma_scale_f32_16x16x128_f8f6f4 v[156:159], v[16:23], v[40:47], v[156:159], v252, v251 op_sel_hi:[0,0,0]
	v_mfma_scale_f32_16x16x128_f8f6f4 v[148:151], v[24:31], v[40:47], v[148:151], v252, v251 op_sel_hi:[0,0,0]
	v_mfma_scale_f32_16x16x128_f8f6f4 v[140:143], v[16:23], v[32:39], v[140:143], v252, v251 op_sel_hi:[0,0,0]
	v_mfma_scale_f32_16x16x128_f8f6f4 v[132:135], v[24:31], v[32:39], v[132:135], v252, v251 op_sel_hi:[0,0,0]
	s_setprio 0
	s_setprio 1
	v_mfma_scale_f32_16x16x128_f8f6f4 v[184:187], v[0:7], v[56:63], v[184:187], v252, v251 op_sel_hi:[0,0,0]
	v_mfma_scale_f32_16x16x128_f8f6f4 v[176:179], v[8:15], v[56:63], v[176:179], v252, v251 op_sel_hi:[0,0,0]
	v_mfma_scale_f32_16x16x128_f8f6f4 v[168:171], v[0:7], v[48:55], v[168:171], v252, v251 op_sel_hi:[0,0,0]
	v_mfma_scale_f32_16x16x128_f8f6f4 v[160:163], v[8:15], v[48:55], v[160:163], v252, v251 op_sel_hi:[0,0,0]
	v_mfma_scale_f32_16x16x128_f8f6f4 v[152:155], v[0:7], v[40:47], v[152:155], v252, v251 op_sel_hi:[0,0,0]
	v_mfma_scale_f32_16x16x128_f8f6f4 v[144:147], v[8:15], v[40:47], v[144:147], v252, v251 op_sel_hi:[0,0,0]
	v_mfma_scale_f32_16x16x128_f8f6f4 v[136:139], v[0:7], v[32:39], v[136:139], v252, v251 op_sel_hi:[0,0,0]
	v_mfma_scale_f32_16x16x128_f8f6f4 v[128:131], v[8:15], v[32:39], v[128:131], v252, v251 op_sel_hi:[0,0,0]
	s_setprio 0
	s_barrier
	s_mov_b32 m0, s34
	v_lshl_add_u64 v[196:197], s[14:15], 0, v[204:205]
	ds_read_b128 v[32:35], v238 offset:16384
	ds_read_b128 v[36:39], v238 offset:17408
	ds_read_b128 v[40:43], v238 offset:18432
	ds_read_b128 v[44:47], v238 offset:19456
	ds_read_b128 v[48:51], v238 offset:20480
	ds_read_b128 v[52:55], v238 offset:21504
	ds_read_b128 v[56:59], v238 offset:22528
	ds_read_b128 v[60:63], v238 offset:23552
	global_load_lds_dwordx4 v[196:197], off
	v_lshl_add_u64 v[198:199], s[14:15], 0, v[208:209]
	s_mov_b32 m0, s35
	v_lshl_add_u64 v[200:201], s[14:15], 0, v[206:207]
	global_load_lds_dwordx4 v[198:199], off
	s_mov_b32 m0, s40
	v_lshl_add_u64 v[202:203], s[14:15], 0, v[210:211]
	global_load_lds_dwordx4 v[200:201], off
	s_mov_b32 m0, s41
	v_mov_b32_e32 v215, v193
	global_load_lds_dwordx4 v[202:203], off
	s_mov_b32 m0, s31
	v_lshl_add_u64 v[226:227], s[12:13], 0, v[192:193]
	global_load_lds_dwordx4 v192, s[12:13]
	s_mov_b32 m0, s53
	v_lshl_add_u64 v[228:229], s[12:13], 0, v[214:215]
	global_load_lds_dwordx4 v214, s[12:13]
	s_waitcnt vmcnt(8)
	s_waitcnt lgkmcnt(0)
	s_barrier
	s_setprio 1
	s_waitcnt lgkmcnt(0)
	s_cmp_eq_u32 s101, 0
	s_cbranch_scc1 .Lpad_gu_4
	v_mfma_scale_f32_16x16x128_f8f6f4 v[124:127], v[16:23], v[32:39], v[124:127], v252, v251 op_sel_hi:[0,0,0]
	v_mfma_scale_f32_16x16x128_f8f6f4 v[116:119], v[24:31], v[32:39], v[116:119], v252, v251 op_sel_hi:[0,0,0]
	v_mfma_scale_f32_16x16x128_f8f6f4 v[108:111], v[16:23], v[40:47], v[108:111], v252, v251 op_sel_hi:[0,0,0]
	v_mfma_scale_f32_16x16x128_f8f6f4 v[100:103], v[24:31], v[40:47], v[100:103], v252, v251 op_sel_hi:[0,0,0]
	v_mfma_scale_f32_16x16x128_f8f6f4 v[92:95], v[16:23], v[48:55], v[92:95], v252, v251 op_sel_hi:[0,0,0]
	v_mfma_scale_f32_16x16x128_f8f6f4 v[84:87], v[24:31], v[48:55], v[84:87], v252, v251 op_sel_hi:[0,0,0]
	v_mfma_scale_f32_16x16x128_f8f6f4 v[76:79], v[16:23], v[56:63], v[76:79], v252, v251 op_sel_hi:[0,0,0]
	v_mfma_scale_f32_16x16x128_f8f6f4 v[68:71], v[24:31], v[56:63], v[68:71], v252, v251 op_sel_hi:[0,0,0]
.Lpad_gu_4:
	s_setprio 0
	s_setprio 1
	s_cmp_eq_u32 s101, 0
	s_cbranch_scc1 .Lpad_gu_5
	v_mfma_scale_f32_16x16x128_f8f6f4 v[120:123], v[0:7], v[32:39], v[120:123], v252, v251 op_sel_hi:[0,0,0]
	v_mfma_scale_f32_16x16x128_f8f6f4 v[112:115], v[8:15], v[32:39], v[112:115], v252, v251 op_sel_hi:[0,0,0]
	v_mfma_scale_f32_16x16x128_f8f6f4 v[104:107], v[0:7], v[40:47], v[104:107], v252, v251 op_sel_hi:[0,0,0]
	v_mfma_scale_f32_16x16x128_f8f6f4 v[96:99], v[8:15], v[40:47], v[96:99], v252, v251 op_sel_hi:[0,0,0]
	v_mfma_scale_f32_16x16x128_f8f6f4 v[88:91], v[0:7], v[48:55], v[88:91], v252, v251 op_sel_hi:[0,0,0]
	v_mfma_scale_f32_16x16x128_f8f6f4 v[80:83], v[8:15], v[48:55], v[80:83], v252, v251 op_sel_hi:[0,0,0]
	v_mfma_scale_f32_16x16x128_f8f6f4 v[72:75], v[0:7], v[56:63], v[72:75], v252, v251 op_sel_hi:[0,0,0]
	v_mfma_scale_f32_16x16x128_f8f6f4 v[64:67], v[8:15], v[56:63], v[64:67], v252, v251 op_sel_hi:[0,0,0]

; #define PG8_WAIT_V(n) asm volatile("s_waitcnt vmcnt(" #n ")" ::: "memory")
; #define PG8_WAIT_L(n) asm volatile("s_waitcnt lgkmcnt(" #n ")" ::: "memory")
; #define PG8_BAR __builtin_amdgcn_s_barrier()
; #define PG8_SCHED __builtin_amdgcn_sched_barrier(0)
; template <class Epi, class Sched, bool GATHER, bool FP8 = false, bool ALIGN = true>
; __device__ __forceinline__ void gemm_phase(LAS unsigned char* lds, int wave, const Gemm g, const Sched& S, const Epi& E) {
;     ...
;             PG8_WAIT_V(8); PG8_WAIT_L(0); PG8_BAR; PG8_MMA(1, 0, At, B0); PG8_MMA(1, 1, At, B1); PG8_BAR; PG8_SCHED;
;         }
.Lpad_gu_7:
	s_setprio 0
	s_barrier
	s_add_i32 s83, s83, 2
	s_add_u32 s10, s10, 0x100
	s_addc_u32 s11, s11, 0
	s_add_u32 s49, s49, 0x100
	s_addc_u32 s82, s82, 0
	s_cmp_gt_u32 s83, 13
	s_cbranch_scc1 .LBB0_1083

; #define PG8_STAGE(bufoff, gbase, voff) do { _Pragma("unroll") for (int _i = 0; _i < 2; ++_i) \
;         __builtin_amdgcn_global_load_lds((const unsigned*)((const char*)(gbase) + (voff)[_i]), (LAS unsigned*)(lds + (bufoff) + ldsw + _i * 8192), 16, 0, 0); } while (0)
; #define PG8_WAIT_V(n) asm volatile("s_waitcnt vmcnt(" #n ")" ::: "memory")
; #define PG8_BAR __builtin_amdgcn_s_barrier()
; #define PG8_AOFF(u_, o0, o1) do { _Pragma("unroll") for (int _i = 0; _i < 2; ++_i) { const int r0 = (u_).pm * BM + Rr[_i], r1 = r0 + HALF; \
;         const int g0 = GATHER ? g.rowidx[r0] : r0, g1 = GATHER ? g.rowidx[r1] : r1; \
;         o0[_i] = (unsigned)g0 * (unsigned)K + (unsigned)Cc[_i]; o1[_i] = (unsigned)g1 * (unsigned)K + (unsigned)Cc[_i]; } } while (0)
; #define REP(j) for (int rep_ = 0; rep_ < 1 + (((REPMASK) >> (j)) & 1); ++rep_)
; template <class Epi, class Sched, bool GATHER, bool FP8 = false, bool ALIGN = true>
; __device__ __forceinline__ void gemm_phase(LAS unsigned char* lds, int wave, const Gemm g, const Sched& S, const Epi& E) {
;     ...
;     PG8_AOFF(cur, ca0, ca1);
;     const char* Ab = (const char*)g.A;
;     const char* cB = (const char*)g.Bt + (size_t)cur.e * g.b_estride + (size_t)cur.pn * tstep;
;     PG8_STAGE(PG8_SB(0, 0), cB, voffB0); PG8_STAGE(PG8_SB(0, 1), cB, voffB1); PG8_STAGE(PG8_SA(0, 0), Ab, ca0); PG8_STAGE(PG8_SA(0, 1), Ab, ca1);
;     if (wr == 1) PG8_BAR;
;     PG8_WAIT_V(2); PG8_BAR;
;     PG8_STAGE(PG8_SB(1, 0), cB + kstep, voffB0); PG8_STAGE(PG8_SA(1, 0), Ab + kstep, ca0); PG8_STAGE(PG8_SB(1, 1), cB + kstep, voffB1);
;     PG8_WAIT_V(6); PG8_BAR;
; __global__ void __launch_bounds__(NTHR, 2) fwd(Args args) {
;     ...
;             if (DOWN_FP8 && l >= FP8_FIRST) {
;                 gm::Gemm g{HB_, ws + WS_WDN + (size_t)l * NE1 * D * DEXP * 2, DEXP, nullptr, (size_t)D * DEXP};
;                 gm::GroupOrder S{tp, 8, Fp.G, Fp.vcu, 0};
;                 gm::EpiStore<true> E{YS_, D, YS8SCALE / W8SCALE};
;                 REP(8) { S.ecur = 0; gm::gemm_phase<gm::EpiStore<true>, gm::GroupOrder, false, true>(Fp.lds, Fp.wave, g, S, E); }
.LBB0_1147:
	s_add_u32 s98, s36, 0x400000
	s_addc_u32 s99, s37, 0
	s_add_u32 s10, s36, 0x68100000
	s_addc_u32 s11, s37, 0
	s_and_b32 s5, s12, 3
	s_add_u32 s14, s36, 0x5e100080
	v_mov_b32_e32 v205, v193
	s_addc_u32 s15, s37, 0
	v_lshl_add_u64 v[6:7], s[48:49], 0, v[204:205]
	v_mov_b32_e32 v209, v193
	s_cmp_lt_u32 s12, 4
	v_lshl_add_u64 v[8:9], s[48:49], 0, v[208:209]
	s_cselect_b64 s[36:37], -1, 0
	v_lshl_add_u64 v[6:7], v[6:7], 0, s[62:63]
	s_add_i32 m0, s31, 0x18000
	v_mov_b32_e32 v213, v193
	s_waitcnt vmcnt(2)
	s_barrier
	global_load_lds_dwordx4 v[6:7], off
	v_lshl_add_u64 v[6:7], v[8:9], 0, s[62:63]
	s_add_i32 m0, s31, 0x1a000
	s_add_i32 s57, s31, 0x8000
	v_mov_b32_e32 v207, v193
	v_mov_b32_e32 v215, v193
	global_load_lds_dwordx4 v[6:7], off
	v_lshl_add_u64 v[6:7], s[14:15], 0, v[212:213]
	s_mov_b32 m0, s57
	s_add_i32 s58, s31, 0xa000
	v_lshl_add_u64 v[10:11], s[48:49], 0, v[206:207]
	v_mov_b32_e32 v211, v193
	global_load_lds_dwordx4 v[6:7], off
	v_lshl_add_u64 v[6:7], s[14:15], 0, v[214:215]
	s_mov_b32 m0, s58
	v_lshl_add_u64 v[12:13], s[48:49], 0, v[210:211]
	global_load_lds_dwordx4 v[6:7], off
	v_lshl_add_u64 v[6:7], v[10:11], 0, s[62:63]
	s_add_i32 m0, s31, 0x1c000
	v_and_b32_e32 v14, 15, v0
	global_load_lds_dwordx4 v[6:7], off
	v_lshl_add_u64 v[6:7], v[12:13], 0, s[62:63]
	s_add_i32 m0, s31, 0x1e000
	v_and_b32_e32 v15, 48, v0
	global_load_lds_dwordx4 v[6:7], off
	v_lshl_or_b32 v235, s13, 6, v14
	v_and_b32_e32 v5, 0xfffffc00, v5
	v_lshl_or_b32 v14, v14, 6, v15
	v_lshlrev_b32_e32 v15, 2, v0
	v_lshl_add_u32 v16, s13, 13, v5
	v_and_b32_e32 v15, 32, v15
	s_waitcnt vmcnt(6)
	v_bitop3_b32 v16, v14, v16, v15 bitop3:0xde
	v_lshl_add_u32 v5, s5, 12, v5
	v_and_b32_e32 v0, -16, v0
	v_bitop3_b32 v236, v14, v5, v15 bitop3:0xde
	v_lshl_add_u32 v237, s5, 6, v0
	v_add_u32_e32 v238, v1, v3
	v_add_u32_e32 v239, v2, v4
	s_mov_b32 s59, 0
	v_add_u32_e32 v240, 0, v16
	s_barrier
	s_branch .LBB0_1150

; #define PG8_STAGE(bufoff, gbase, voff) do { _Pragma("unroll") for (int _i = 0; _i < 2; ++_i) \
;         __builtin_amdgcn_global_load_lds((const unsigned*)((const char*)(gbase) + (voff)[_i]), (LAS unsigned*)(lds + (bufoff) + ldsw + _i * 8192), 16, 0, 0); } while (0)
; #define PG8_LDA(dst, b, h) do { _Pragma("unroll") for (int m = 0; m < 4; ++m) _Pragma("unroll") for (int k = 0; k < 2; ++k) dst[m][k] = *(const LAS bf16x8*)(lds + PG8_SA(b, h) + aoff + m * 2048 + k * KOFF); } while (0)
; #define PG8_LDB(dst, b, h) do { _Pragma("unroll") for (int n = 0; n < 2; ++n) _Pragma("unroll") for (int k = 0; k < 2; ++k) dst[n][k] = *(const LAS bf16x8*)(lds + PG8_SB(b, h) + boff + n * 2048 + k * KOFF); } while (0)
; #define PG8_SCHED __builtin_amdgcn_sched_barrier(0)
; #define PG8_AOFF(u_, o0, o1) do { _Pragma("unroll") for (int _i = 0; _i < 2; ++_i) { const int r0 = (u_).pm * BM + Rr[_i], r1 = r0 + HALF; \
;         const int g0 = GATHER ? g.rowidx[r0] : r0, g1 = GATHER ? g.rowidx[r1] : r1; \
;         o0[_i] = (unsigned)g0 * (unsigned)K + (unsigned)Cc[_i]; o1[_i] = (unsigned)g1 * (unsigned)K + (unsigned)Cc[_i]; } } while (0)
; template <class Epi, class Sched, bool GATHER, bool FP8 = false, bool ALIGN = true>
; __device__ __forceinline__ void gemm_phase(LAS unsigned char* lds, int wave, const Gemm g, const Sched& S, const Epi& E) {
;     ...
;             const bool last = (t == nt - 2);
;             const char* a1 = Ab + (size_t)(t + 1) * kstep;
;             const char* a2 = last ? Ab : Ab + (size_t)(t + 2) * kstep; const char* b2 = last ? nB : cB + (size_t)(t + 2) * kstep;
;             const char* a3 = a2 + kstep; const char* b3 = b2 + kstep;
;             PG8_LDB(B0, 0, 0); PG8_LDB(B1, 0, 1); PG8_SCHED; PG8_LDA(At, 0, 0); PG8_STAGE(PG8_SA(1, 1), a1, ca1);
;             if (last && has_next) PG8_AOFF(nxt, ca0, ca1);
.Lpeel_dn_h:
	v_readlane_b32 s100, v255, 7
	s_lshr_b32 s100, s100, 2
	s_lshl_b32 s100, s100, 8
	s_lshl_b32 s101, s73, 10
	s_add_u32 s100, s100, s101
	s_add_u32 s100, s100, 0x200
	s_add_u32 s100, s98, s100
	s_addc_u32 s101, s99, 0
	v_mov_b32_e32 v244, s100
	v_mov_b32_e32 v245, s101
	global_load_dword v246, v[244:245], off
	v_add_u32_e32 v0, 0, v236
	v_add_u32_e32 v1, 0x10000, v0
	v_add_u32_e32 v12, 0x14000, v0
	ds_read_b128 v[16:19], v1
	ds_read_b128 v[20:23], v1 offset:1024
	ds_read_b128 v[24:27], v1 offset:2048
	ds_read_b128 v[28:31], v1 offset:3072
	ds_read_b128 v[0:3], v12
	ds_read_b128 v[4:7], v12 offset:1024
	ds_read_b128 v[8:11], v12 offset:2048
	ds_read_b128 v[12:15], v12 offset:3072
	s_add_u32 s12, s6, s82
	s_addc_u32 s13, s7, s83
	v_lshl_add_u64 v[196:197], s[12:13], 0, v[192:193]
	v_lshl_add_u64 v[196:197], v[196:197], 0, s[62:63]
	s_add_i32 m0, s31, 0xc000
	v_mov_b32_e32 v217, v193
	ds_read_b128 v[56:59], v240
	ds_read_b128 v[60:63], v240 offset:1024
	ds_read_b128 v[48:51], v240 offset:2048
	ds_read_b128 v[52:55], v240 offset:3072
	ds_read_b128 v[40:43], v240 offset:4096
	ds_read_b128 v[44:47], v240 offset:5120
	ds_read_b128 v[32:35], v240 offset:6144
	ds_read_b128 v[36:39], v240 offset:7168
	global_load_lds_dwordx4 v[196:197], off
	v_lshl_add_u64 v[196:197], s[12:13], 0, v[216:217]
	v_lshl_add_u64 v[196:197], v[196:197], 0, s[62:63]
	s_add_i32 m0, s31, 0xe000
	s_and_b64 s[14:15], s[42:43], s[80:81]
	global_load_lds_dwordx4 v[196:197], off
	s_andn2_b64 vcc, exec, s[14:15]
	s_cbranch_vccnz .Lpeel_dn_a
	v_mov_b64_e32 v[222:223], v[220:221]
	v_mov_b64_e32 v[224:225], v[218:219]
	v_mov_b32_e32 v214, v242
	v_mov_b32_e32 v212, v241
	v_mov_b32_e32 v216, v220
	v_mov_b32_e32 v192, v218
	s_branch .Lpeel_dn_b

; #define PG8_STAGE(bufoff, gbase, voff) do { _Pragma("unroll") for (int _i = 0; _i < 2; ++_i) \
;         __builtin_amdgcn_global_load_lds((const unsigned*)((const char*)(gbase) + (voff)[_i]), (LAS unsigned*)(lds + (bufoff) + ldsw + _i * 8192), 16, 0, 0); } while (0)
; #define PG8_LDA(dst, b, h) do { _Pragma("unroll") for (int m = 0; m < 4; ++m) _Pragma("unroll") for (int k = 0; k < 2; ++k) dst[m][k] = *(const LAS bf16x8*)(lds + PG8_SA(b, h) + aoff + m * 2048 + k * KOFF); } while (0)
; #define PG8_LDB(dst, b, h) do { _Pragma("unroll") for (int n = 0; n < 2; ++n) _Pragma("unroll") for (int k = 0; k < 2; ++k) dst[n][k] = *(const LAS bf16x8*)(lds + PG8_SB(b, h) + boff + n * 2048 + k * KOFF); } while (0)
; #define PG8_WAIT_V(n) asm volatile("s_waitcnt vmcnt(" #n ")" ::: "memory")
; #define PG8_WAIT_L(n) asm volatile("s_waitcnt lgkmcnt(" #n ")" ::: "memory")
; #define PG8_BAR __builtin_amdgcn_s_barrier()
; #define PG8_SCHED __builtin_amdgcn_sched_barrier(0)
; #define PG8_AOFF(u_, o0, o1) do { _Pragma("unroll") for (int _i = 0; _i < 2; ++_i) { const int r0 = (u_).pm * BM + Rr[_i], r1 = r0 + HALF; \
;         const int g0 = GATHER ? g.rowidx[r0] : r0, g1 = GATHER ? g.rowidx[r1] : r1; \
;         o0[_i] = (unsigned)g0 * (unsigned)K + (unsigned)Cc[_i]; o1[_i] = (unsigned)g1 * (unsigned)K + (unsigned)Cc[_i]; } } while (0)
; template <class Epi, class Sched, bool GATHER, bool FP8 = false, bool ALIGN = true>
; __device__ __forceinline__ void gemm_phase(LAS unsigned char* lds, int wave, const Gemm g, const Sched& S, const Epi& E) {
;     ...
;             PG8_LDB(B0, 0, 0); PG8_LDB(B1, 0, 1); PG8_SCHED; PG8_LDA(At, 0, 0); PG8_STAGE(PG8_SA(1, 1), a1, ca1);
;             if (last && has_next) PG8_AOFF(nxt, ca0, ca1);
;             PG8_WAIT_V(8); PG8_WAIT_L(0); PG8_BAR; PG8_MMA(0, 0, At, B0); PG8_MMA(0, 1, At, B1); PG8_BAR; PG8_SCHED;
;             PG8_LDA(At, 0, 1); PG8_STAGE(PG8_SB(0, 0), b2, voffB0); PG8_STAGE(PG8_SB(0, 1), b2, voffB1); PG8_STAGE(PG8_SA(0, 0), a2, ca0);
;             PG8_WAIT_V(8); PG8_WAIT_L(0); PG8_BAR; PG8_MMA(1, 0, At, B0); PG8_MMA(1, 1, At, B1); PG8_BAR; PG8_SCHED;
.Lpeel_dn_b:
	s_xor_b64 s[50:51], s[84:85], -1
	s_add_u32 s14, s12, 0x100
	s_addc_u32 s15, s13, 0
	s_and_b64 s[12:13], s[80:81], exec
	s_cselect_b32 s13, s7, s15
	s_cselect_b32 s12, s6, s14
	s_add_u32 s14, s48, s82
	s_addc_u32 s15, s49, s83
	s_waitcnt vmcnt(8)
	s_add_u32 s79, s14, 0x100
	s_waitcnt lgkmcnt(0)
	s_addc_u32 s82, s15, 0
	s_and_b64 s[14:15], s[80:81], exec
	s_cselect_b32 s15, s5, s82
	s_cselect_b32 s14, s39, s79
	s_barrier
	s_setprio 1
	s_waitcnt lgkmcnt(0)
	v_mfma_scale_f32_16x16x128_f8f6f4 v[188:191], v[16:23], v[56:63], 0, v252, v251 op_sel_hi:[0,0,0]
	v_mfma_scale_f32_16x16x128_f8f6f4 v[184:187], v[24:31], v[56:63], 0, v252, v251 op_sel_hi:[0,0,0]
	v_mfma_scale_f32_16x16x128_f8f6f4 v[172:175], v[16:23], v[48:55], 0, v252, v251 op_sel_hi:[0,0,0]
	v_mfma_scale_f32_16x16x128_f8f6f4 v[168:171], v[24:31], v[48:55], 0, v252, v251 op_sel_hi:[0,0,0]
	v_mfma_scale_f32_16x16x128_f8f6f4 v[156:159], v[16:23], v[40:47], 0, v252, v251 op_sel_hi:[0,0,0]
	v_mfma_scale_f32_16x16x128_f8f6f4 v[152:155], v[24:31], v[40:47], 0, v252, v251 op_sel_hi:[0,0,0]
	v_mfma_scale_f32_16x16x128_f8f6f4 v[140:143], v[16:23], v[32:39], 0, v252, v251 op_sel_hi:[0,0,0]
	v_mfma_scale_f32_16x16x128_f8f6f4 v[136:139], v[24:31], v[32:39], 0, v252, v251 op_sel_hi:[0,0,0]
	s_setprio 0
	s_setprio 1
	v_mfma_scale_f32_16x16x128_f8f6f4 v[180:183], v[0:7], v[56:63], 0, v252, v251 op_sel_hi:[0,0,0]
	v_mfma_scale_f32_16x16x128_f8f6f4 v[176:179], v[8:15], v[56:63], 0, v252, v251 op_sel_hi:[0,0,0]
	v_mfma_scale_f32_16x16x128_f8f6f4 v[164:167], v[0:7], v[48:55], 0, v252, v251 op_sel_hi:[0,0,0]
	v_mfma_scale_f32_16x16x128_f8f6f4 v[160:163], v[8:15], v[48:55], 0, v252, v251 op_sel_hi:[0,0,0]
	v_mfma_scale_f32_16x16x128_f8f6f4 v[148:151], v[0:7], v[40:47], 0, v252, v251 op_sel_hi:[0,0,0]
	v_mfma_scale_f32_16x16x128_f8f6f4 v[144:147], v[8:15], v[40:47], 0, v252, v251 op_sel_hi:[0,0,0]
	v_mfma_scale_f32_16x16x128_f8f6f4 v[132:135], v[0:7], v[32:39], 0, v252, v251 op_sel_hi:[0,0,0]
	v_mfma_scale_f32_16x16x128_f8f6f4 v[128:131], v[8:15], v[32:39], 0, v252, v251 op_sel_hi:[0,0,0]
	s_setprio 0
	s_barrier
	s_mov_b32 m0, s34
	v_lshl_add_u64 v[196:197], s[14:15], 0, v[204:205]
	ds_read_b128 v[32:35], v240 offset:16384
	ds_read_b128 v[36:39], v240 offset:17408
	ds_read_b128 v[40:43], v240 offset:18432
	ds_read_b128 v[44:47], v240 offset:19456
	ds_read_b128 v[48:51], v240 offset:20480
	ds_read_b128 v[52:55], v240 offset:21504
	ds_read_b128 v[56:59], v240 offset:22528
	ds_read_b128 v[60:63], v240 offset:23552
	global_load_lds_dwordx4 v[196:197], off
	v_lshl_add_u64 v[198:199], s[14:15], 0, v[208:209]
	s_mov_b32 m0, s35
	v_lshl_add_u64 v[200:201], s[14:15], 0, v[206:207]
	global_load_lds_dwordx4 v[198:199], off
	s_mov_b32 m0, s40
	v_lshl_add_u64 v[202:203], s[14:15], 0, v[210:211]
	global_load_lds_dwordx4 v[200:201], off
	s_mov_b32 m0, s41
	v_mov_b32_e32 v213, v193
	global_load_lds_dwordx4 v[202:203], off
	s_mov_b32 m0, s31
	v_mov_b32_e32 v215, v193
	global_load_lds_dwordx4 v212, s[12:13]
	s_mov_b32 m0, s47
	v_lshl_add_u64 v[226:227], s[12:13], 0, v[212:213]
	global_load_lds_dwordx4 v214, s[12:13]
	s_waitcnt vmcnt(8)
	s_waitcnt lgkmcnt(0)
	v_lshl_add_u64 v[228:229], s[12:13], 0, v[214:215]
	s_barrier
	s_setprio 1
	s_waitcnt lgkmcnt(0)
	v_readfirstlane_b32 s101, v246
	s_cmp_eq_u32 s101, 0
	s_cbranch_scc1 .Lpad_dn_0
	v_mfma_scale_f32_16x16x128_f8f6f4 v[124:127], v[16:23], v[32:39], 0, v252, v251 op_sel_hi:[0,0,0]
	v_mfma_scale_f32_16x16x128_f8f6f4 v[120:123], v[24:31], v[32:39], 0, v252, v251 op_sel_hi:[0,0,0]
	v_mfma_scale_f32_16x16x128_f8f6f4 v[108:111], v[16:23], v[40:47], 0, v252, v251 op_sel_hi:[0,0,0]
	v_mfma_scale_f32_16x16x128_f8f6f4 v[104:107], v[24:31], v[40:47], 0, v252, v251 op_sel_hi:[0,0,0]
	v_mfma_scale_f32_16x16x128_f8f6f4 v[92:95], v[16:23], v[48:55], 0, v252, v251 op_sel_hi:[0,0,0]
	v_mfma_scale_f32_16x16x128_f8f6f4 v[88:91], v[24:31], v[48:55], 0, v252, v251 op_sel_hi:[0,0,0]
	v_mfma_scale_f32_16x16x128_f8f6f4 v[76:79], v[16:23], v[56:63], 0, v252, v251 op_sel_hi:[0,0,0]
	v_mfma_scale_f32_16x16x128_f8f6f4 v[72:75], v[24:31], v[56:63], 0, v252, v251 op_sel_hi:[0,0,0]
.Lpad_dn_0:
	s_setprio 0
	s_setprio 1
	s_cmp_eq_u32 s101, 0
	s_cbranch_scc1 .Lpad_dn_1
	v_mfma_scale_f32_16x16x128_f8f6f4 v[116:119], v[0:7], v[32:39], 0, v252, v251 op_sel_hi:[0,0,0]
	v_mfma_scale_f32_16x16x128_f8f6f4 v[112:115], v[8:15], v[32:39], 0, v252, v251 op_sel_hi:[0,0,0]
	v_mfma_scale_f32_16x16x128_f8f6f4 v[100:103], v[0:7], v[40:47], 0, v252, v251 op_sel_hi:[0,0,0]
	v_mfma_scale_f32_16x16x128_f8f6f4 v[96:99], v[8:15], v[40:47], 0, v252, v251 op_sel_hi:[0,0,0]
	v_mfma_scale_f32_16x16x128_f8f6f4 v[84:87], v[0:7], v[48:55], 0, v252, v251 op_sel_hi:[0,0,0]
	v_mfma_scale_f32_16x16x128_f8f6f4 v[80:83], v[8:15], v[48:55], 0, v252, v251 op_sel_hi:[0,0,0]
	v_mfma_scale_f32_16x16x128_f8f6f4 v[68:71], v[0:7], v[56:63], 0, v252, v251 op_sel_hi:[0,0,0]
	v_mfma_scale_f32_16x16x128_f8f6f4 v[64:67], v[8:15], v[56:63], 0, v252, v251 op_sel_hi:[0,0,0]
; #define PG8_STAGE(bufoff, gbase, voff) do { _Pragma("unroll") for (int _i = 0; _i < 2; ++_i) \
;         __builtin_amdgcn_global_load_lds((const unsigned*)((const char*)(gbase) + (voff)[_i]), (LAS unsigned*)(lds + (bufoff) + ldsw + _i * 8192), 16, 0, 0); } while (0)
; #define PG8_LDA(dst, b, h) do { _Pragma("unroll") for (int m = 0; m < 4; ++m) _Pragma("unroll") for (int k = 0; k < 2; ++k) dst[m][k] = *(const LAS bf16x8*)(lds + PG8_SA(b, h) + aoff + m * 2048 + k * KOFF); } while (0)
; #define PG8_LDB(dst, b, h) do { _Pragma("unroll") for (int n = 0; n < 2; ++n) _Pragma("unroll") for (int k = 0; k < 2; ++k) dst[n][k] = *(const LAS bf16x8*)(lds + PG8_SB(b, h) + boff + n * 2048 + k * KOFF); } while (0)
; #define PG8_WAIT_V(n) asm volatile("s_waitcnt vmcnt(" #n ")" ::: "memory")
; #define PG8_WAIT_L(n) asm volatile("s_waitcnt lgkmcnt(" #n ")" ::: "memory")
; #define PG8_BAR __builtin_amdgcn_s_barrier()
; #define PG8_SCHED __builtin_amdgcn_sched_barrier(0)
; template <class Epi, class Sched, bool GATHER, bool FP8 = false, bool ALIGN = true>
; __device__ __forceinline__ void gemm_phase(LAS unsigned char* lds, int wave, const Gemm g, const Sched& S, const Epi& E) {
;     ...
;             PG8_LDB(B0, 1, 0); PG8_LDB(B1, 1, 1); PG8_SCHED; PG8_LDA(At, 1, 0); PG8_STAGE(PG8_SA(0, 1), a2, ca1);
;             PG8_WAIT_V(8); PG8_WAIT_L(0); PG8_BAR; PG8_MMA(0, 0, At, B0); PG8_MMA(0, 1, At, B1); PG8_BAR; PG8_SCHED;
;             PG8_LDA(At, 1, 1); PG8_STAGE(PG8_SB(1, 0), b3, voffB0); PG8_STAGE(PG8_SB(1, 1), b3, voffB1); PG8_STAGE(PG8_SA(1, 0), a3, ca0);
;             PG8_WAIT_V(8); PG8_WAIT_L(0); PG8_BAR; PG8_MMA(1, 0, At, B0); PG8_MMA(1, 1, At, B1); PG8_BAR; PG8_SCHED;
.Lpad_dn_1:
	s_setprio 0
	s_barrier
	s_add_i32 s14, 0, 0x18000
	s_add_i32 s15, 0, 0x1c000
	v_add_u32_e32 v12, s14, v236
	v_add_u32_e32 v28, s15, v236
	ds_read_b128 v[0:3], v12
	ds_read_b128 v[4:7], v12 offset:1024
	ds_read_b128 v[8:11], v12 offset:2048
	ds_read_b128 v[12:15], v12 offset:3072
	ds_read_b128 v[16:19], v28
	ds_read_b128 v[20:23], v28 offset:1024
	ds_read_b128 v[24:27], v28 offset:2048
	ds_read_b128 v[28:31], v28 offset:3072
	s_mov_b32 m0, s53
	v_lshl_add_u64 v[224:225], s[12:13], 0, v[224:225]
	ds_read_b128 v[32:35], v240 offset:32768
	ds_read_b128 v[36:39], v240 offset:33792
	ds_read_b128 v[40:43], v240 offset:34816
	ds_read_b128 v[44:47], v240 offset:35840
	ds_read_b128 v[48:51], v240 offset:36864
	ds_read_b128 v[52:55], v240 offset:37888
	ds_read_b128 v[56:59], v240 offset:38912
	ds_read_b128 v[60:63], v240 offset:39936
	global_load_lds_dwordx4 v[224:225], off
	v_lshl_add_u64 v[222:223], s[12:13], 0, v[222:223]
	s_mov_b32 m0, s56
	s_nop 0
	global_load_lds_dwordx4 v[222:223], off
	s_waitcnt vmcnt(8)
	s_waitcnt lgkmcnt(0)
	s_barrier
	s_setprio 1
	s_waitcnt lgkmcnt(0)
	v_mfma_scale_f32_16x16x128_f8f6f4 v[188:191], v[0:7], v[32:39], v[188:191], v252, v251 op_sel_hi:[0,0,0]
	v_mfma_scale_f32_16x16x128_f8f6f4 v[184:187], v[8:15], v[32:39], v[184:187], v252, v251 op_sel_hi:[0,0,0]
	v_mfma_scale_f32_16x16x128_f8f6f4 v[172:175], v[0:7], v[40:47], v[172:175], v252, v251 op_sel_hi:[0,0,0]
	v_mfma_scale_f32_16x16x128_f8f6f4 v[168:171], v[8:15], v[40:47], v[168:171], v252, v251 op_sel_hi:[0,0,0]
	v_mfma_scale_f32_16x16x128_f8f6f4 v[156:159], v[0:7], v[48:55], v[156:159], v252, v251 op_sel_hi:[0,0,0]
	v_mfma_scale_f32_16x16x128_f8f6f4 v[152:155], v[8:15], v[48:55], v[152:155], v252, v251 op_sel_hi:[0,0,0]
	v_mfma_scale_f32_16x16x128_f8f6f4 v[140:143], v[0:7], v[56:63], v[140:143], v252, v251 op_sel_hi:[0,0,0]
	v_mfma_scale_f32_16x16x128_f8f6f4 v[136:139], v[8:15], v[56:63], v[136:139], v252, v251 op_sel_hi:[0,0,0]
	s_setprio 0
	s_setprio 1
	v_mfma_scale_f32_16x16x128_f8f6f4 v[180:183], v[16:23], v[32:39], v[180:183], v252, v251 op_sel_hi:[0,0,0]
	v_mfma_scale_f32_16x16x128_f8f6f4 v[176:179], v[24:31], v[32:39], v[176:179], v252, v251 op_sel_hi:[0,0,0]
	v_mfma_scale_f32_16x16x128_f8f6f4 v[164:167], v[16:23], v[40:47], v[164:167], v252, v251 op_sel_hi:[0,0,0]
	v_mfma_scale_f32_16x16x128_f8f6f4 v[160:163], v[24:31], v[40:47], v[160:163], v252, v251 op_sel_hi:[0,0,0]
	v_mfma_scale_f32_16x16x128_f8f6f4 v[148:151], v[16:23], v[48:55], v[148:151], v252, v251 op_sel_hi:[0,0,0]
	v_mfma_scale_f32_16x16x128_f8f6f4 v[144:147], v[24:31], v[48:55], v[144:147], v252, v251 op_sel_hi:[0,0,0]
	v_mfma_scale_f32_16x16x128_f8f6f4 v[132:135], v[16:23], v[56:63], v[132:135], v252, v251 op_sel_hi:[0,0,0]
	v_mfma_scale_f32_16x16x128_f8f6f4 v[128:131], v[24:31], v[56:63], v[128:131], v252, v251 op_sel_hi:[0,0,0]
	s_setprio 0
	s_barrier
	s_add_i32 s12, s14, s30
	v_lshl_add_u64 v[196:197], v[196:197], 0, s[62:63]
	s_mov_b32 m0, s12
	ds_read_b128 v[32:35], v240 offset:49152
	ds_read_b128 v[36:39], v240 offset:50176
	ds_read_b128 v[40:43], v240 offset:51200
	ds_read_b128 v[44:47], v240 offset:52224
	ds_read_b128 v[48:51], v240 offset:53248
	ds_read_b128 v[52:55], v240 offset:54272
	ds_read_b128 v[56:59], v240 offset:55296
	ds_read_b128 v[60:63], v240 offset:56320
	global_load_lds_dwordx4 v[196:197], off
	v_lshl_add_u64 v[196:197], v[198:199], 0, s[62:63]
	s_add_i32 m0, s12, 0x2000
	s_add_i32 s12, s15, s30
	global_load_lds_dwordx4 v[196:197], off
	v_lshl_add_u64 v[196:197], v[200:201], 0, s[62:63]
	s_mov_b32 m0, s12
	s_nop 0
	global_load_lds_dwordx4 v[196:197], off
	v_lshl_add_u64 v[196:197], v[202:203], 0, s[62:63]
	s_add_i32 m0, s12, 0x2000
	s_nop 0
	global_load_lds_dwordx4 v[196:197], off
	v_lshl_add_u64 v[196:197], v[226:227], 0, s[62:63]
	s_mov_b32 m0, s57
	s_nop 0
	global_load_lds_dwordx4 v[196:197], off
	v_lshl_add_u64 v[196:197], v[228:229], 0, s[62:63]
	s_mov_b32 m0, s58
	s_nop 0
	global_load_lds_dwordx4 v[196:197], off
	s_waitcnt vmcnt(8)
	s_waitcnt lgkmcnt(0)
	s_barrier
	s_setprio 1
	s_waitcnt lgkmcnt(0)
	s_cmp_eq_u32 s101, 0
	s_cbranch_scc1 .Lpad_dn_2
	v_mfma_scale_f32_16x16x128_f8f6f4 v[124:127], v[0:7], v[32:39], v[124:127], v252, v251 op_sel_hi:[0,0,0]
	v_mfma_scale_f32_16x16x128_f8f6f4 v[120:123], v[8:15], v[32:39], v[120:123], v252, v251 op_sel_hi:[0,0,0]
	v_mfma_scale_f32_16x16x128_f8f6f4 v[108:111], v[0:7], v[40:47], v[108:111], v252, v251 op_sel_hi:[0,0,0]
	v_mfma_scale_f32_16x16x128_f8f6f4 v[104:107], v[8:15], v[40:47], v[104:107], v252, v251 op_sel_hi:[0,0,0]
	v_mfma_scale_f32_16x16x128_f8f6f4 v[92:95], v[0:7], v[48:55], v[92:95], v252, v251 op_sel_hi:[0,0,0]
	v_mfma_scale_f32_16x16x128_f8f6f4 v[88:91], v[8:15], v[48:55], v[88:91], v252, v251 op_sel_hi:[0,0,0]
	v_mfma_scale_f32_16x16x128_f8f6f4 v[76:79], v[0:7], v[56:63], v[76:79], v252, v251 op_sel_hi:[0,0,0]
	v_mfma_scale_f32_16x16x128_f8f6f4 v[72:75], v[8:15], v[56:63], v[72:75], v252, v251 op_sel_hi:[0,0,0]
.Lpad_dn_2:
	s_setprio 0
	s_setprio 1
	s_cmp_eq_u32 s101, 0
	s_cbranch_scc1 .Lpad_dn_3
	v_mfma_scale_f32_16x16x128_f8f6f4 v[116:119], v[16:23], v[32:39], v[116:119], v252, v251 op_sel_hi:[0,0,0]
	v_mfma_scale_f32_16x16x128_f8f6f4 v[112:115], v[24:31], v[32:39], v[112:115], v252, v251 op_sel_hi:[0,0,0]
	v_mfma_scale_f32_16x16x128_f8f6f4 v[100:103], v[16:23], v[40:47], v[100:103], v252, v251 op_sel_hi:[0,0,0]
	v_mfma_scale_f32_16x16x128_f8f6f4 v[96:99], v[24:31], v[40:47], v[96:99], v252, v251 op_sel_hi:[0,0,0]
	v_mfma_scale_f32_16x16x128_f8f6f4 v[84:87], v[16:23], v[48:55], v[84:87], v252, v251 op_sel_hi:[0,0,0]
	v_mfma_scale_f32_16x16x128_f8f6f4 v[80:83], v[24:31], v[48:55], v[80:83], v252, v251 op_sel_hi:[0,0,0]
	v_mfma_scale_f32_16x16x128_f8f6f4 v[68:71], v[16:23], v[56:63], v[68:71], v252, v251 op_sel_hi:[0,0,0]
	v_mfma_scale_f32_16x16x128_f8f6f4 v[64:67], v[24:31], v[56:63], v[64:67], v252, v251 op_sel_hi:[0,0,0]
.Lpad_dn_3:
	s_setprio 0
	s_barrier
	s_mov_b64 s[84:85], 0
	s_mov_b64 s[80:81], -1
	s_and_b64 vcc, exec, s[50:51]
	s_cbranch_vccnz .LBB0_1160
	s_mov_b64 s[82:83], 0x100
	s_branch .LBB0_1155

; #define PG8_STAGE(bufoff, gbase, voff) do { _Pragma("unroll") for (int _i = 0; _i < 2; ++_i) \
;         __builtin_amdgcn_global_load_lds((const unsigned*)((const char*)(gbase) + (voff)[_i]), (LAS unsigned*)(lds + (bufoff) + ldsw + _i * 8192), 16, 0, 0); } while (0)
; #define PG8_LDA(dst, b, h) do { _Pragma("unroll") for (int m = 0; m < 4; ++m) _Pragma("unroll") for (int k = 0; k < 2; ++k) dst[m][k] = *(const LAS bf16x8*)(lds + PG8_SA(b, h) + aoff + m * 2048 + k * KOFF); } while (0)
; #define PG8_LDB(dst, b, h) do { _Pragma("unroll") for (int n = 0; n < 2; ++n) _Pragma("unroll") for (int k = 0; k < 2; ++k) dst[n][k] = *(const LAS bf16x8*)(lds + PG8_SB(b, h) + boff + n * 2048 + k * KOFF); } while (0)
; #define PG8_WAIT_V(n) asm volatile("s_waitcnt vmcnt(" #n ")" ::: "memory")
; #define PG8_WAIT_L(n) asm volatile("s_waitcnt lgkmcnt(" #n ")" ::: "memory")
; #define PG8_BAR __builtin_amdgcn_s_barrier()
; #define PG8_SCHED __builtin_amdgcn_sched_barrier(0)
; #define PG8_AOFF(u_, o0, o1) do { _Pragma("unroll") for (int _i = 0; _i < 2; ++_i) { const int r0 = (u_).pm * BM + Rr[_i], r1 = r0 + HALF; \
;         const int g0 = GATHER ? g.rowidx[r0] : r0, g1 = GATHER ? g.rowidx[r1] : r1; \
;         o0[_i] = (unsigned)g0 * (unsigned)K + (unsigned)Cc[_i]; o1[_i] = (unsigned)g1 * (unsigned)K + (unsigned)Cc[_i]; } } while (0)
; template <class Epi, class Sched, bool GATHER, bool FP8 = false, bool ALIGN = true>
; __device__ __forceinline__ void gemm_phase(LAS unsigned char* lds, int wave, const Gemm g, const Sched& S, const Epi& E) {
;     ...
;             PG8_LDB(B0, 0, 0); PG8_LDB(B1, 0, 1); PG8_SCHED; PG8_LDA(At, 0, 0); PG8_STAGE(PG8_SA(1, 1), a1, ca1);
;             if (last && has_next) PG8_AOFF(nxt, ca0, ca1);
;             PG8_WAIT_V(8); PG8_WAIT_L(0); PG8_BAR; PG8_MMA(0, 0, At, B0); PG8_MMA(0, 1, At, B1); PG8_BAR; PG8_SCHED;
;             PG8_LDA(At, 0, 1); PG8_STAGE(PG8_SB(0, 0), b2, voffB0); PG8_STAGE(PG8_SB(0, 1), b2, voffB1); PG8_STAGE(PG8_SA(0, 0), a2, ca0);
;             PG8_WAIT_V(8); PG8_WAIT_L(0); PG8_BAR; PG8_MMA(1, 0, At, B0); PG8_MMA(1, 1, At, B1); PG8_BAR; PG8_SCHED;
.LBB0_1158:
	s_xor_b64 s[50:51], s[84:85], -1
	s_add_u32 s14, s12, 0x100
	s_addc_u32 s15, s13, 0
	s_and_b64 s[12:13], s[80:81], exec
	s_cselect_b32 s13, s7, s15
	s_cselect_b32 s12, s6, s14
	s_add_u32 s14, s48, s82
	s_addc_u32 s15, s49, s83
	s_waitcnt vmcnt(8)
	s_add_u32 s79, s14, 0x100
	s_waitcnt lgkmcnt(0)
	s_addc_u32 s82, s15, 0
	s_and_b64 s[14:15], s[80:81], exec
	s_cselect_b32 s15, s5, s82
	s_cselect_b32 s14, s39, s79
	s_barrier
	s_setprio 1
	s_waitcnt lgkmcnt(0)
	v_mfma_scale_f32_16x16x128_f8f6f4 v[188:191], v[16:23], v[56:63], v[188:191], v252, v251 op_sel_hi:[0,0,0]
	v_mfma_scale_f32_16x16x128_f8f6f4 v[184:187], v[24:31], v[56:63], v[184:187], v252, v251 op_sel_hi:[0,0,0]
	v_mfma_scale_f32_16x16x128_f8f6f4 v[172:175], v[16:23], v[48:55], v[172:175], v252, v251 op_sel_hi:[0,0,0]
	v_mfma_scale_f32_16x16x128_f8f6f4 v[168:171], v[24:31], v[48:55], v[168:171], v252, v251 op_sel_hi:[0,0,0]
	v_mfma_scale_f32_16x16x128_f8f6f4 v[156:159], v[16:23], v[40:47], v[156:159], v252, v251 op_sel_hi:[0,0,0]
	v_mfma_scale_f32_16x16x128_f8f6f4 v[152:155], v[24:31], v[40:47], v[152:155], v252, v251 op_sel_hi:[0,0,0]
	v_mfma_scale_f32_16x16x128_f8f6f4 v[140:143], v[16:23], v[32:39], v[140:143], v252, v251 op_sel_hi:[0,0,0]
	v_mfma_scale_f32_16x16x128_f8f6f4 v[136:139], v[24:31], v[32:39], v[136:139], v252, v251 op_sel_hi:[0,0,0]
	s_setprio 0
	s_setprio 1
	v_mfma_scale_f32_16x16x128_f8f6f4 v[180:183], v[0:7], v[56:63], v[180:183], v252, v251 op_sel_hi:[0,0,0]
	v_mfma_scale_f32_16x16x128_f8f6f4 v[176:179], v[8:15], v[56:63], v[176:179], v252, v251 op_sel_hi:[0,0,0]
	v_mfma_scale_f32_16x16x128_f8f6f4 v[164:167], v[0:7], v[48:55], v[164:167], v252, v251 op_sel_hi:[0,0,0]
	v_mfma_scale_f32_16x16x128_f8f6f4 v[160:163], v[8:15], v[48:55], v[160:163], v252, v251 op_sel_hi:[0,0,0]
	v_mfma_scale_f32_16x16x128_f8f6f4 v[148:151], v[0:7], v[40:47], v[148:151], v252, v251 op_sel_hi:[0,0,0]
	v_mfma_scale_f32_16x16x128_f8f6f4 v[144:147], v[8:15], v[40:47], v[144:147], v252, v251 op_sel_hi:[0,0,0]
	v_mfma_scale_f32_16x16x128_f8f6f4 v[132:135], v[0:7], v[32:39], v[132:135], v252, v251 op_sel_hi:[0,0,0]
	v_mfma_scale_f32_16x16x128_f8f6f4 v[128:131], v[8:15], v[32:39], v[128:131], v252, v251 op_sel_hi:[0,0,0]
	s_setprio 0
	s_barrier
	s_mov_b32 m0, s34
	v_lshl_add_u64 v[196:197], s[14:15], 0, v[204:205]
	ds_read_b128 v[32:35], v240 offset:16384
	ds_read_b128 v[36:39], v240 offset:17408
	ds_read_b128 v[40:43], v240 offset:18432
	ds_read_b128 v[44:47], v240 offset:19456
	ds_read_b128 v[48:51], v240 offset:20480
	ds_read_b128 v[52:55], v240 offset:21504
	ds_read_b128 v[56:59], v240 offset:22528
	ds_read_b128 v[60:63], v240 offset:23552
	global_load_lds_dwordx4 v[196:197], off
	v_lshl_add_u64 v[198:199], s[14:15], 0, v[208:209]
	s_mov_b32 m0, s35
	v_lshl_add_u64 v[200:201], s[14:15], 0, v[206:207]
	global_load_lds_dwordx4 v[198:199], off
	s_mov_b32 m0, s40
	v_lshl_add_u64 v[202:203], s[14:15], 0, v[210:211]
	global_load_lds_dwordx4 v[200:201], off
	s_mov_b32 m0, s41
	v_mov_b32_e32 v213, v193
	global_load_lds_dwordx4 v[202:203], off
	s_mov_b32 m0, s31
	v_mov_b32_e32 v215, v193
	global_load_lds_dwordx4 v212, s[12:13]
	s_mov_b32 m0, s47
	v_lshl_add_u64 v[226:227], s[12:13], 0, v[212:213]
	global_load_lds_dwordx4 v214, s[12:13]
	s_waitcnt vmcnt(8)
	s_waitcnt lgkmcnt(0)
	v_lshl_add_u64 v[228:229], s[12:13], 0, v[214:215]
	s_barrier
	s_setprio 1
	s_waitcnt lgkmcnt(0)
	s_cmp_eq_u32 s101, 0
	s_cbranch_scc1 .Lpad_dn_4
	v_mfma_scale_f32_16x16x128_f8f6f4 v[124:127], v[16:23], v[32:39], v[124:127], v252, v251 op_sel_hi:[0,0,0]
	v_mfma_scale_f32_16x16x128_f8f6f4 v[120:123], v[24:31], v[32:39], v[120:123], v252, v251 op_sel_hi:[0,0,0]
	v_mfma_scale_f32_16x16x128_f8f6f4 v[108:111], v[16:23], v[40:47], v[108:111], v252, v251 op_sel_hi:[0,0,0]
	v_mfma_scale_f32_16x16x128_f8f6f4 v[104:107], v[24:31], v[40:47], v[104:107], v252, v251 op_sel_hi:[0,0,0]
	v_mfma_scale_f32_16x16x128_f8f6f4 v[92:95], v[16:23], v[48:55], v[92:95], v252, v251 op_sel_hi:[0,0,0]
	v_mfma_scale_f32_16x16x128_f8f6f4 v[88:91], v[24:31], v[48:55], v[88:91], v252, v251 op_sel_hi:[0,0,0]
	v_mfma_scale_f32_16x16x128_f8f6f4 v[76:79], v[16:23], v[56:63], v[76:79], v252, v251 op_sel_hi:[0,0,0]
	v_mfma_scale_f32_16x16x128_f8f6f4 v[72:75], v[24:31], v[56:63], v[72:75], v252, v251 op_sel_hi:[0,0,0]
.Lpad_dn_4:
	s_setprio 0
	s_setprio 1
	s_cmp_eq_u32 s101, 0
	s_cbranch_scc1 .Lpad_dn_5
	v_mfma_scale_f32_16x16x128_f8f6f4 v[116:119], v[0:7], v[32:39], v[116:119], v252, v251 op_sel_hi:[0,0,0]
	v_mfma_scale_f32_16x16x128_f8f6f4 v[112:115], v[8:15], v[32:39], v[112:115], v252, v251 op_sel_hi:[0,0,0]
	v_mfma_scale_f32_16x16x128_f8f6f4 v[100:103], v[0:7], v[40:47], v[100:103], v252, v251 op_sel_hi:[0,0,0]
	v_mfma_scale_f32_16x16x128_f8f6f4 v[96:99], v[8:15], v[40:47], v[96:99], v252, v251 op_sel_hi:[0,0,0]
	v_mfma_scale_f32_16x16x128_f8f6f4 v[84:87], v[0:7], v[48:55], v[84:87], v252, v251 op_sel_hi:[0,0,0]
	v_mfma_scale_f32_16x16x128_f8f6f4 v[80:83], v[8:15], v[48:55], v[80:83], v252, v251 op_sel_hi:[0,0,0]
	v_mfma_scale_f32_16x16x128_f8f6f4 v[68:71], v[0:7], v[56:63], v[68:71], v252, v251 op_sel_hi:[0,0,0]
	v_mfma_scale_f32_16x16x128_f8f6f4 v[64:67], v[8:15], v[56:63], v[64:67], v252, v251 op_sel_hi:[0,0,0]
